# down GEMM: first two super-phase waits allow the 8 epilogue stores to stay in flight (vmcnt 16), phase prologue drains fully
# speedup vs baseline: 1.0047x; 1.0047x over previous
; #define PG8_STAGEA(bufoff, gbase, h) do { if constexpr (GATHER) { PG8_STAGE(bufoff, gbase, vA[h]); } else { PG8_STAGE(bufoff, (gbase) + (h) * hstepA, voffA); } } while (0)
; #define PG8_WAIT_V(n) asm volatile("s_waitcnt vmcnt(" #n ")" ::: "memory")
; #define PG8_BAR __builtin_amdgcn_s_barrier()
; #define PG8_CALCA(u, vo) do { _Pragma("unroll") for (int _h = 0; _h < 2; ++_h) _Pragma("unroll") for (int _i = 0; _i < 2; ++_i) \
;         vo[_h][_i] = Sched::ABLK ? ((unsigned)S.arow(u, 0) * (unsigned)lda + voffA[_i] + (unsigned)_h * 8192u) : ((unsigned)S.arow(u, _h * HALF + Rr[_i]) * (unsigned)lda + C2[_i]); } while (0)
;     __device__ __forceinline__ int arow(const pg8::Unit& u, int r) const { if (GATHER && u.roff >= 0) { const int rr = r < u.nvalid ? r : u.nvalid - 1; return tokl[u.roff + rr]; } return -u.roff - 1 + r; }
; template <class Epi, class Sched>
; __device__ __forceinline__ void gemm_phase(const int tid, LAS unsigned char* lds, const char* Abase, const int lda, const int ldb, const int K, const Sched& S, const Epi& E) {
;     ...
;     if constexpr (GATHER) { PG8_CALCA(cur, vA); } else { cA = Abase + (size_t)S.arow(cur, 0) * lda + S.acolb(cur); }
;     const char* cB = cur.bptr;
;     PG8_STAGE(PG8_SB(0, 0), cB, voffB); PG8_STAGE(PG8_SB(0, 1), cB + hstepB, voffB); PG8_STAGEA(PG8_SA(0, 0), cA, 0); PG8_STAGEA(PG8_SA(0, 1), cA, 1);
;     if (wr == 1) PG8_BAR;
;     PG8_WAIT_V(2); PG8_BAR;
;     PG8_STAGE(PG8_SB(1, 0), cB + kstep, voffB); PG8_STAGEA(PG8_SA(1, 0), cA + kstepA, 0); PG8_STAGE(PG8_SB(1, 1), cB + hstepB + kstep, voffB);
;     PG8_WAIT_V(6); PG8_BAR;
.LBB0_1696:
	s_add_u32 s44, s40, 0x29a00000
	s_addc_u32 s45, s41, 0
	s_lshl_b32 s40, s51, 11
	s_add_i32 s40, s40, 0
	s_and_b32 s52, s46, 3
	s_mov_b32 s85, s51
	s_add_i32 s51, s40, 0x24000
	s_lshl_b32 s46, s50, 13
	s_lshl_b32 s47, s52, 12
	s_add_u32 s40, s56, 0x80
	v_mov_b32_e32 v1, v3
	s_addc_u32 s41, s57, 0
	s_add_i32 m0, s25, 0x18000
	v_lshl_add_u64 v[4:5], s[40:41], 0, v[0:1]
	v_mov_b32_e32 v197, v3
	s_waitcnt vmcnt(2)
	s_barrier
	global_load_lds_dwordx4 v[4:5], off
	s_add_i32 m0, s25, 0x1a000
	v_lshl_add_u64 v[4:5], s[40:41], 0, v[196:197]
	s_add_u32 s40, s2, 0x8000
	v_mov_b32_e32 v201, v3
	s_addc_u32 s41, s3, 0
	s_add_i32 s73, s25, 0x8000
	v_mov_b32_e32 v199, v3
	global_load_lds_dwordx4 v[4:5], off
	v_lshl_add_u64 v[4:5], s[40:41], 0, v[200:201]
	s_mov_b32 m0, s73
	s_add_i32 s76, s25, 0xa000
	global_load_lds_dwordx4 v[4:5], off
	v_lshl_add_u64 v[4:5], s[40:41], 0, v[198:199]
	s_add_u32 s40, s56, 0x2080
	s_mov_b32 m0, s76
	s_addc_u32 s41, s57, 0
	global_load_lds_dwordx4 v[4:5], off
	s_add_i32 m0, s25, 0x1c000
	v_lshl_add_u64 v[4:5], s[40:41], 0, v[0:1]
	global_load_lds_dwordx4 v[4:5], off
	v_lshl_add_u64 v[4:5], s[40:41], 0, v[196:197]
	s_add_i32 m0, s25, 0x1e000
	v_lshlrev_b32_e32 v6, 6, v251
	global_load_lds_dwordx4 v[4:5], off
	v_bfe_u32 v5, v251, 4, 2
	v_and_b32_e32 v6, 0x3c0, v6
	v_lshlrev_b32_e32 v8, 2, v251
	v_lshrrev_b32_e32 v4, 4, v251
	v_lshl_or_b32 v7, v5, 4, v6
	v_and_b32_e32 v8, 32, v8
	v_and_b32_e32 v10, 3, v251
	v_and_b32_e32 v11, 7, v251
	v_bitop3_b32 v9, v7, s46, v8 bitop3:0xde
	v_bitop3_b32 v199, s47, v7, v8 bitop3:0xf6
	s_cmp_gt_i32 s5, 0
	v_lshrrev_b32_e32 v7, 2, v251
	v_bitop3_b32 v4, v4, v11, 3 bitop3:0x6c
	v_bitop3_b32 v5, v5, v11, 4 bitop3:0x36
	v_lshlrev_b32_e32 v11, 1, v10
	v_bfe_u32 v12, v251, 2, 3
	s_waitcnt vmcnt(0)
	s_cselect_b64 s[46:47], -1, 0
	s_add_i32 s78, s5, -2
	v_bfe_u32 v8, v251, 2, 4
	v_bitop3_b32 v7, v7, v11, 7 bitop3:0x6c
	v_bitop3_b32 v11, v11, v12, 1 bitop3:0x36
	s_cmpk_lt_u32 s48, 0x100
	v_lshlrev_b32_e32 v4, 3, v4
	v_lshlrev_b32_e32 v5, 3, v5
	v_lshlrev_b32_e32 v7, 3, v7
	v_lshlrev_b32_e32 v11, 3, v11
	v_lshl_or_b32 v201, s50, 6, v8
	v_add_u32_e32 v6, s51, v6
	v_lshl_add_u32 v8, v8, 6, s51
	v_readlane_b32 s40, v253, 57
	s_mov_b32 s77, 0
	s_cselect_b64 s[48:49], -1, 0
	s_lshl_b32 s79, s52, 6
	v_lshlrev_b32_e32 v204, 4, v10
	v_mov_b32_e32 v205, v3
	v_add_u32_e32 v239, v6, v4
	v_add_u32_e32 v240, v6, v5
	v_add_u32_e32 v241, v8, v7
	v_add_u32_e32 v242, v8, v11
	v_add_u32_e32 v243, 0, v9
	s_mov_b32 s86, s40
	s_barrier
	v_readlane_b32 s41, v253, 58
	s_branch .LBB0_1699

; #define PG8_STAGEA(bufoff, gbase, h) do { if constexpr (GATHER) { PG8_STAGE(bufoff, gbase, vA[h]); } else { PG8_STAGE(bufoff, (gbase) + (h) * hstepA, voffA); } } while (0)
; #define PG8_LDA(dst, b, h) do { _Pragma("unroll") for (int m = 0; m < 4; ++m) _Pragma("unroll") for (int k = 0; k < 2; ++k) dst[m][k] = *(const LAS bf16x8*)(lds + PG8_SA(b, h) + aoff + m * 2048 + k * 1024); } while (0)
; #define PG8_MM(ai, bj, At, Bt) do { if constexpr (Epi::F8MMA) PG8_MMA8(ai, bj, At, Bt##8); else PG8_MMA(ai, bj, At, Bt); } while (0)
; #define PG8_WAIT_V(n) asm volatile("s_waitcnt vmcnt(" #n ")" ::: "memory")
; #define PG8_WAIT_L(n) asm volatile("s_waitcnt lgkmcnt(" #n ")" ::: "memory")
; #define PG8_BAR __builtin_amdgcn_s_barrier()
; #define PG8_SCHED __builtin_amdgcn_sched_barrier(0)
; template <class Epi, class Sched>
; __device__ __forceinline__ void gemm_phase(const int tid, LAS unsigned char* lds, const char* Abase, const int lda, const int ldb, const int K, const Sched& S, const Epi& E) {
;     ...
;             PG8_LDB(B0, 0, 0); PG8_LDB(B1, 0, 1); PG8_SCHED; PG8_LDA(At, 0, 0); PG8_STAGEA(PG8_SA(1, 1), a1, 1);
;             if constexpr (GATHER) { if (last) {
; #pragma unroll
;                 for (int h = 0; h < 2; ++h)
; #pragma unroll
;                     for (int i = 0; i < 2; ++i) vA[h][i] = vAn[h][i]; } }
;             PG8_WAIT_V(8); PG8_WAIT_L(0); PG8_BAR; PG8_MM(0, 0, At, B0); PG8_MM(0, 1, At, B1); PG8_BAR; PG8_SCHED;
;             PG8_LDA(At, 0, 1); PG8_STAGE(PG8_SB(0, 0), b2, voffB); PG8_STAGE(PG8_SB(0, 1), b2 + hstepB, voffB); PG8_STAGEA(PG8_SA(0, 0), a2, 0);
;             PG8_WAIT_V(8); PG8_WAIT_L(0); PG8_BAR; PG8_MM(1, 0, At, B0); PG8_MM(1, 1, At, B1); PG8_BAR; PG8_SCHED;
.LBB0_1708:
	s_add_i32 s89, s89, 2
	s_and_b64 s[60:61], s[62:63], exec
	s_cselect_b32 s61, 0, s56
	s_cselect_b32 s60, 0, s57
	s_add_u32 s66, s2, s61
	s_addc_u32 s67, s3, s60
	s_add_u32 s60, s66, 0x8000
	s_addc_u32 s61, s67, 0
	s_waitcnt vmcnt(16)
	s_and_b64 s[62:63], s[62:63], exec
	s_waitcnt lgkmcnt(0)
	s_cselect_b32 s62, s54, s87
	s_cselect_b32 s63, s55, s88
	s_add_u32 s64, s62, 0x80
	s_addc_u32 s65, s63, 0
	s_barrier
	s_setprio 1
	s_waitcnt lgkmcnt(0)
	v_mfma_scale_f32_16x16x128_f8f6f4 v[192:195], v[20:27], v[60:67], 0, v224, v216 op_sel_hi:[0,0,0]
	v_mfma_scale_f32_16x16x128_f8f6f4 v[188:191], v[28:35], v[60:67], 0, v224, v216 op_sel_hi:[0,0,0]
	v_mfma_scale_f32_16x16x128_f8f6f4 v[176:179], v[20:27], v[52:59], 0, v224, v216 op_sel_hi:[0,0,0]
	v_mfma_scale_f32_16x16x128_f8f6f4 v[172:175], v[28:35], v[52:59], 0, v224, v216 op_sel_hi:[0,0,0]
	v_mfma_scale_f32_16x16x128_f8f6f4 v[160:163], v[20:27], v[44:51], 0, v224, v216 op_sel_hi:[0,0,0]
	v_mfma_scale_f32_16x16x128_f8f6f4 v[156:159], v[28:35], v[44:51], 0, v224, v216 op_sel_hi:[0,0,0]
	v_mfma_scale_f32_16x16x128_f8f6f4 v[144:147], v[20:27], v[36:43], 0, v224, v216 op_sel_hi:[0,0,0]
	v_mfma_scale_f32_16x16x128_f8f6f4 v[140:143], v[28:35], v[36:43], 0, v224, v216 op_sel_hi:[0,0,0]
	s_setprio 0
	s_setprio 1
	v_mfma_scale_f32_16x16x128_f8f6f4 v[184:187], v[4:11], v[60:67], 0, v224, v216 op_sel_hi:[0,0,0]
	v_mfma_scale_f32_16x16x128_f8f6f4 v[180:183], v[12:19], v[60:67], 0, v224, v216 op_sel_hi:[0,0,0]
	v_mfma_scale_f32_16x16x128_f8f6f4 v[168:171], v[4:11], v[52:59], 0, v224, v216 op_sel_hi:[0,0,0]
	v_mfma_scale_f32_16x16x128_f8f6f4 v[164:167], v[12:19], v[52:59], 0, v224, v216 op_sel_hi:[0,0,0]
	v_mfma_scale_f32_16x16x128_f8f6f4 v[152:155], v[4:11], v[44:51], 0, v224, v216 op_sel_hi:[0,0,0]
	v_mfma_scale_f32_16x16x128_f8f6f4 v[148:151], v[12:19], v[44:51], 0, v224, v216 op_sel_hi:[0,0,0]
	v_mfma_scale_f32_16x16x128_f8f6f4 v[136:139], v[4:11], v[36:43], 0, v224, v216 op_sel_hi:[0,0,0]
	v_mfma_scale_f32_16x16x128_f8f6f4 v[132:135], v[12:19], v[36:43], 0, v224, v216 op_sel_hi:[0,0,0]
	s_setprio 0
	s_barrier
	s_mov_b32 m0, s28
	v_lshl_add_u64 v[228:229], s[62:63], 0, v[0:1]
	s_add_u32 s90, s62, 0x2000
	ds_read_b128 v[36:39], v243 offset:16384
	ds_read_b128 v[40:43], v243 offset:17408
	ds_read_b128 v[44:47], v243 offset:18432
	ds_read_b128 v[48:51], v243 offset:19456
	ds_read_b128 v[52:55], v243 offset:20480
	ds_read_b128 v[56:59], v243 offset:21504
	ds_read_b128 v[60:63], v243 offset:22528
	ds_read_b128 v[64:67], v243 offset:23552
	global_load_lds_dwordx4 v[228:229], off
	v_lshl_add_u64 v[228:229], s[62:63], 0, v[196:197]
	s_mov_b32 m0, s29
	s_addc_u32 s91, s63, 0
	global_load_lds_dwordx4 v[228:229], off
	v_lshl_add_u64 v[228:229], s[90:91], 0, v[0:1]
	s_mov_b32 m0, s68
	s_nop 0
	global_load_lds_dwordx4 v[228:229], off
	v_lshl_add_u64 v[228:229], s[90:91], 0, v[196:197]
	s_mov_b32 m0, s69
	s_nop 0
	global_load_lds_dwordx4 v[228:229], off
	s_mov_b32 m0, s25
	s_nop 0
	global_load_lds_dwordx4 v200, s[66:67]
	s_mov_b32 m0, s70
	s_nop 0
	global_load_lds_dwordx4 v198, s[66:67]
	s_waitcnt vmcnt(16)
	s_waitcnt lgkmcnt(0)
	s_barrier
	s_setprio 1
	s_waitcnt lgkmcnt(0)
	v_mfma_scale_f32_16x16x128_f8f6f4 v[128:131], v[20:27], v[36:43], 0, v224, v216 op_sel_hi:[0,0,0]
	v_mfma_scale_f32_16x16x128_f8f6f4 v[124:127], v[28:35], v[36:43], 0, v224, v216 op_sel_hi:[0,0,0]
	v_mfma_scale_f32_16x16x128_f8f6f4 v[112:115], v[20:27], v[44:51], 0, v224, v216 op_sel_hi:[0,0,0]
	v_mfma_scale_f32_16x16x128_f8f6f4 v[108:111], v[28:35], v[44:51], 0, v224, v216 op_sel_hi:[0,0,0]
	v_mfma_scale_f32_16x16x128_f8f6f4 v[96:99], v[20:27], v[52:59], 0, v224, v216 op_sel_hi:[0,0,0]
	v_mfma_scale_f32_16x16x128_f8f6f4 v[92:95], v[28:35], v[52:59], 0, v224, v216 op_sel_hi:[0,0,0]
	v_mfma_scale_f32_16x16x128_f8f6f4 v[80:83], v[20:27], v[60:67], 0, v224, v216 op_sel_hi:[0,0,0]
	v_mfma_scale_f32_16x16x128_f8f6f4 v[76:79], v[28:35], v[60:67], 0, v224, v216 op_sel_hi:[0,0,0]
	s_setprio 0
	s_setprio 1
	v_mfma_scale_f32_16x16x128_f8f6f4 v[120:123], v[4:11], v[36:43], 0, v224, v216 op_sel_hi:[0,0,0]
	v_mfma_scale_f32_16x16x128_f8f6f4 v[116:119], v[12:19], v[36:43], 0, v224, v216 op_sel_hi:[0,0,0]
	v_mfma_scale_f32_16x16x128_f8f6f4 v[104:107], v[4:11], v[44:51], 0, v224, v216 op_sel_hi:[0,0,0]
	v_mfma_scale_f32_16x16x128_f8f6f4 v[100:103], v[12:19], v[44:51], 0, v224, v216 op_sel_hi:[0,0,0]
	v_mfma_scale_f32_16x16x128_f8f6f4 v[88:91], v[4:11], v[52:59], 0, v224, v216 op_sel_hi:[0,0,0]
	v_mfma_scale_f32_16x16x128_f8f6f4 v[84:87], v[12:19], v[52:59], 0, v224, v216 op_sel_hi:[0,0,0]
	v_mfma_scale_f32_16x16x128_f8f6f4 v[72:75], v[4:11], v[60:67], 0, v224, v216 op_sel_hi:[0,0,0]
	v_mfma_scale_f32_16x16x128_f8f6f4 v[68:71], v[12:19], v[60:67], 0, v224, v216 op_sel_hi:[0,0,0]
	s_setprio 0
	s_barrier
	s_add_i32 s90, 0, 0x18000
	s_add_i32 s91, 0, 0x1c000
	v_add_u32_e32 v16, s90, v199
	v_add_u32_e32 v32, s91, v199
	ds_read_b128 v[4:7], v16
	ds_read_b128 v[8:11], v16 offset:1024
	ds_read_b128 v[12:15], v16 offset:2048
	ds_read_b128 v[16:19], v16 offset:3072
	ds_read_b128 v[20:23], v32
	ds_read_b128 v[24:27], v32 offset:1024
	ds_read_b128 v[28:31], v32 offset:2048
	ds_read_b128 v[32:35], v32 offset:3072
	s_mov_b32 m0, s71
	v_lshl_add_u64 v[212:213], s[66:67], 0, v[212:213]
	ds_read_b128 v[36:39], v243 offset:32768
	ds_read_b128 v[40:43], v243 offset:33792
	ds_read_b128 v[44:47], v243 offset:34816
	ds_read_b128 v[48:51], v243 offset:35840
	ds_read_b128 v[52:55], v243 offset:36864
	ds_read_b128 v[56:59], v243 offset:37888
	ds_read_b128 v[60:63], v243 offset:38912
	ds_read_b128 v[64:67], v243 offset:39936
	global_load_lds_dwordx4 v[212:213], off
	v_lshl_add_u64 v[210:211], s[66:67], 0, v[210:211]
	s_mov_b32 m0, s72
	s_nop 0
	global_load_lds_dwordx4 v[210:211], off
	s_waitcnt vmcnt(8)
	s_waitcnt lgkmcnt(0)
	s_barrier
; #define PG8_STAGEA(bufoff, gbase, h) do { if constexpr (GATHER) { PG8_STAGE(bufoff, gbase, vA[h]); } else { PG8_STAGE(bufoff, (gbase) + (h) * hstepA, voffA); } } while (0)
; #define PG8_LDA(dst, b, h) do { _Pragma("unroll") for (int m = 0; m < 4; ++m) _Pragma("unroll") for (int k = 0; k < 2; ++k) dst[m][k] = *(const LAS bf16x8*)(lds + PG8_SA(b, h) + aoff + m * 2048 + k * 1024); } while (0)
; #define PG8_MM(ai, bj, At, Bt) do { if constexpr (Epi::F8MMA) PG8_MMA8(ai, bj, At, Bt##8); else PG8_MMA(ai, bj, At, Bt); } while (0)
; #define PG8_WAIT_V(n) asm volatile("s_waitcnt vmcnt(" #n ")" ::: "memory")
; #define PG8_WAIT_L(n) asm volatile("s_waitcnt lgkmcnt(" #n ")" ::: "memory")
; #define PG8_BAR __builtin_amdgcn_s_barrier()
; #define PG8_SCHED __builtin_amdgcn_sched_barrier(0)
; template <class Epi, class Sched>
; __device__ __forceinline__ void gemm_phase(const int tid, LAS unsigned char* lds, const char* Abase, const int lda, const int ldb, const int K, const Sched& S, const Epi& E) {
;     ...
;             PG8_LDB(B0, 1, 0); PG8_LDB(B1, 1, 1); PG8_SCHED; PG8_LDA(At, 1, 0); PG8_STAGEA(PG8_SA(0, 1), a2, 1);
;             PG8_WAIT_V(8); PG8_WAIT_L(0); PG8_BAR; PG8_MM(0, 0, At, B0); PG8_MM(0, 1, At, B1); PG8_BAR; PG8_SCHED;
;             PG8_LDA(At, 1, 1); PG8_STAGE(PG8_SB(1, 0), b3, voffB); PG8_STAGE(PG8_SB(1, 1), b3 + hstepB, voffB); PG8_STAGEA(PG8_SA(1, 0), a3, 0);
;             PG8_WAIT_V(8); PG8_WAIT_L(0); PG8_BAR; PG8_MM(1, 0, At, B0); PG8_MM(1, 1, At, B1); PG8_BAR; PG8_SCHED;
;         }
	s_setprio 1
	s_waitcnt lgkmcnt(0)
	v_mfma_scale_f32_16x16x128_f8f6f4 v[192:195], v[4:11], v[36:43], v[192:195], v224, v216 op_sel_hi:[0,0,0]
	v_mfma_scale_f32_16x16x128_f8f6f4 v[188:191], v[12:19], v[36:43], v[188:191], v224, v216 op_sel_hi:[0,0,0]
	v_mfma_scale_f32_16x16x128_f8f6f4 v[176:179], v[4:11], v[44:51], v[176:179], v224, v216 op_sel_hi:[0,0,0]
	v_mfma_scale_f32_16x16x128_f8f6f4 v[172:175], v[12:19], v[44:51], v[172:175], v224, v216 op_sel_hi:[0,0,0]
	v_mfma_scale_f32_16x16x128_f8f6f4 v[160:163], v[4:11], v[52:59], v[160:163], v224, v216 op_sel_hi:[0,0,0]
	v_mfma_scale_f32_16x16x128_f8f6f4 v[156:159], v[12:19], v[52:59], v[156:159], v224, v216 op_sel_hi:[0,0,0]
	v_mfma_scale_f32_16x16x128_f8f6f4 v[144:147], v[4:11], v[60:67], v[144:147], v224, v216 op_sel_hi:[0,0,0]
	v_mfma_scale_f32_16x16x128_f8f6f4 v[140:143], v[12:19], v[60:67], v[140:143], v224, v216 op_sel_hi:[0,0,0]
	s_setprio 0
	s_setprio 1
	v_mfma_scale_f32_16x16x128_f8f6f4 v[184:187], v[20:27], v[36:43], v[184:187], v224, v216 op_sel_hi:[0,0,0]
	v_mfma_scale_f32_16x16x128_f8f6f4 v[180:183], v[28:35], v[36:43], v[180:183], v224, v216 op_sel_hi:[0,0,0]
	v_mfma_scale_f32_16x16x128_f8f6f4 v[168:171], v[20:27], v[44:51], v[168:171], v224, v216 op_sel_hi:[0,0,0]
	v_mfma_scale_f32_16x16x128_f8f6f4 v[164:167], v[28:35], v[44:51], v[164:167], v224, v216 op_sel_hi:[0,0,0]
	v_mfma_scale_f32_16x16x128_f8f6f4 v[152:155], v[20:27], v[52:59], v[152:155], v224, v216 op_sel_hi:[0,0,0]
	v_mfma_scale_f32_16x16x128_f8f6f4 v[148:151], v[28:35], v[52:59], v[148:151], v224, v216 op_sel_hi:[0,0,0]
	v_mfma_scale_f32_16x16x128_f8f6f4 v[136:139], v[20:27], v[60:67], v[136:139], v224, v216 op_sel_hi:[0,0,0]
	v_mfma_scale_f32_16x16x128_f8f6f4 v[132:135], v[28:35], v[60:67], v[132:135], v224, v216 op_sel_hi:[0,0,0]
	s_setprio 0
	s_barrier
	s_add_i32 s66, s90, s22
	v_lshl_add_u64 v[210:211], s[64:65], 0, v[0:1]
	s_mov_b32 m0, s66
	ds_read_b128 v[36:39], v243 offset:49152
	ds_read_b128 v[40:43], v243 offset:50176
	ds_read_b128 v[44:47], v243 offset:51200
	ds_read_b128 v[48:51], v243 offset:52224
	ds_read_b128 v[52:55], v243 offset:53248
	ds_read_b128 v[56:59], v243 offset:54272
	ds_read_b128 v[60:63], v243 offset:55296
	ds_read_b128 v[64:67], v243 offset:56320
	global_load_lds_dwordx4 v[210:211], off
	s_add_i32 m0, s66, 0x2000
	s_add_u32 s62, s62, 0x2080
	v_lshl_add_u64 v[210:211], s[64:65], 0, v[196:197]
	s_addc_u32 s63, s63, 0
	s_add_i32 s64, s91, s22
	global_load_lds_dwordx4 v[210:211], off
	v_lshl_add_u64 v[210:211], s[62:63], 0, v[0:1]
	s_mov_b32 m0, s64
	s_nop 0
	global_load_lds_dwordx4 v[210:211], off
	v_lshl_add_u64 v[210:211], s[62:63], 0, v[196:197]
	s_add_i32 m0, s64, 0x2000
	s_nop 0
	global_load_lds_dwordx4 v[210:211], off
	s_mov_b32 m0, s73
	s_nop 0
	global_load_lds_dwordx4 v200, s[60:61]
	s_mov_b32 m0, s76
	s_nop 0
	global_load_lds_dwordx4 v198, s[60:61]
	s_waitcnt vmcnt(8)
	s_waitcnt lgkmcnt(0)
	s_barrier
	s_setprio 1
	s_waitcnt lgkmcnt(0)
	v_mfma_scale_f32_16x16x128_f8f6f4 v[128:131], v[4:11], v[36:43], v[128:131], v224, v216 op_sel_hi:[0,0,0]
	v_mfma_scale_f32_16x16x128_f8f6f4 v[124:127], v[12:19], v[36:43], v[124:127], v224, v216 op_sel_hi:[0,0,0]
	v_mfma_scale_f32_16x16x128_f8f6f4 v[112:115], v[4:11], v[44:51], v[112:115], v224, v216 op_sel_hi:[0,0,0]
	v_mfma_scale_f32_16x16x128_f8f6f4 v[108:111], v[12:19], v[44:51], v[108:111], v224, v216 op_sel_hi:[0,0,0]
	v_mfma_scale_f32_16x16x128_f8f6f4 v[96:99], v[4:11], v[52:59], v[96:99], v224, v216 op_sel_hi:[0,0,0]
	v_mfma_scale_f32_16x16x128_f8f6f4 v[92:95], v[12:19], v[52:59], v[92:95], v224, v216 op_sel_hi:[0,0,0]
	v_mfma_scale_f32_16x16x128_f8f6f4 v[80:83], v[4:11], v[60:67], v[80:83], v224, v216 op_sel_hi:[0,0,0]
	v_mfma_scale_f32_16x16x128_f8f6f4 v[76:79], v[12:19], v[60:67], v[76:79], v224, v216 op_sel_hi:[0,0,0]
	s_setprio 0
	s_setprio 1
	v_mfma_scale_f32_16x16x128_f8f6f4 v[120:123], v[20:27], v[36:43], v[120:123], v224, v216 op_sel_hi:[0,0,0]
	v_mfma_scale_f32_16x16x128_f8f6f4 v[116:119], v[28:35], v[36:43], v[116:119], v224, v216 op_sel_hi:[0,0,0]
	v_mfma_scale_f32_16x16x128_f8f6f4 v[104:107], v[20:27], v[44:51], v[104:107], v224, v216 op_sel_hi:[0,0,0]
	v_mfma_scale_f32_16x16x128_f8f6f4 v[100:103], v[28:35], v[44:51], v[100:103], v224, v216 op_sel_hi:[0,0,0]
	v_mfma_scale_f32_16x16x128_f8f6f4 v[88:91], v[20:27], v[52:59], v[88:91], v224, v216 op_sel_hi:[0,0,0]
	v_mfma_scale_f32_16x16x128_f8f6f4 v[84:87], v[28:35], v[52:59], v[84:87], v224, v216 op_sel_hi:[0,0,0]
	v_mfma_scale_f32_16x16x128_f8f6f4 v[72:75], v[20:27], v[60:67], v[72:75], v224, v216 op_sel_hi:[0,0,0]
	v_mfma_scale_f32_16x16x128_f8f6f4 v[68:71], v[28:35], v[60:67], v[68:71], v224, v216 op_sel_hi:[0,0,0]
	s_setprio 0
	s_barrier
	s_add_u32 s87, s87, 0x100
	s_addc_u32 s88, s88, 0
	s_add_u32 s56, s56, 0x10000
	s_addc_u32 s57, s57, 0
	s_cmp_ge_i32 s89, s5
	s_cbranch_scc1 .LBB0_1711
